# v048 + agent-scope (sc1) on prep's streaming input loads (L1 bypass)
# speedup vs baseline: 1.0169x; 1.0046x over previous
.LBB0_5:
	v_lshrrev_b32_e32 v70, 6, v0
	v_and_b32_e32 v1, 63, v0
	v_lshlrev_b32_e32 v10, 1, v70
	v_or_b32_e32 v4, 8, v70
	v_lshlrev_b32_e32 v54, 4, v1
	v_mov_b32_e32 v55, 0
	v_mul_u32_u24_e32 v2, s6, v10
	v_lshlrev_b32_e32 v11, 1, v4
	v_lshl_add_u64 v[56:57], s[8:9], 0, v[54:55]
	v_lshlrev_b32_e32 v2, 2, v2
	v_mov_b32_e32 v3, v55
	v_mul_u32_u24_e32 v4, s6, v11
	v_lshl_add_u64 v[2:3], v[56:57], 0, v[2:3]
	v_lshlrev_b32_e32 v4, 2, v4
	v_mov_b32_e32 v5, v55
	v_lshl_add_u64 v[4:5], v[56:57], 0, v[4:5]
	global_load_dwordx4 v[18:21], v[2:3], off sc1
	global_load_dwordx4 v[6:9], v[4:5], off sc1
	v_or_b32_e32 v2, 1, v10
	v_mul_u32_u24_e32 v2, s6, v2
	v_lshlrev_b32_e32 v2, 2, v2
	v_mov_b32_e32 v3, v55
	v_lshl_add_u64 v[2:3], v[56:57], 0, v[2:3]
	global_load_dwordx4 v[14:17], v[2:3], off sc1
	v_or_b32_e32 v2, 1, v11
	v_mul_hi_u32_u24_e32 v3, s6, v2
	v_mul_u32_u24_e32 v2, s6, v2
	v_lshl_add_u64 v[2:3], v[2:3], 2, v[56:57]
	global_load_dwordx4 v[2:5], v[2:3], off sc1
	v_or_b32_e32 v10, 4, v70
	v_or_b32_e32 v12, 12, v70
	v_lshlrev_b32_e32 v50, 1, v10
	v_lshlrev_b32_e32 v68, 1, v12
	v_mul_u32_u24_e32 v10, s6, v50
	v_mov_b32_e32 v11, v55
	v_mul_u32_u24_e32 v12, s6, v68
	v_lshlrev_b32_e32 v10, 2, v10
	v_mov_b32_e32 v13, v55
	v_lshlrev_b32_e32 v12, 2, v12
	v_lshl_add_u64 v[10:11], v[56:57], 0, v[10:11]
	global_load_dwordx4 v[42:45], v[10:11], off sc1
	v_lshl_add_u64 v[10:11], v[56:57], 0, v[12:13]
	v_or_b32_e32 v26, 16, v70
	global_load_dwordx4 v[22:25], v[10:11], off sc1
	v_or_b32_e32 v10, 24, v70
	v_lshlrev_b32_e32 v12, 1, v26
	v_lshlrev_b32_e32 v10, 1, v10
	v_mul_u32_u24_e32 v13, s6, v12
	v_or_b32_e32 v12, 1, v12
	v_mul_u32_u24_e32 v28, s6, v10
	v_or_b32_e32 v30, 1, v10
	v_lshlrev_b32_e32 v26, 2, v13
	v_mul_hi_u32_u24_e32 v13, s6, v12
	v_mul_u32_u24_e32 v12, s6, v12
	v_mov_b32_e32 v27, v55
	v_mov_b32_e32 v11, v55
	v_lshlrev_b32_e32 v10, 2, v28
	v_mul_hi_u32_u24_e32 v29, s6, v30
	v_mul_u32_u24_e32 v28, s6, v30
	v_lshl_add_u64 v[32:33], v[12:13], 2, v[56:57]
	v_lshl_add_u64 v[30:31], v[56:57], 0, v[26:27]
	v_lshl_add_u64 v[46:47], v[56:57], 0, v[10:11]
	v_lshl_add_u64 v[48:49], v[28:29], 2, v[56:57]
	global_load_dwordx4 v[34:37], v[32:33], off sc1
	global_load_dwordx4 v[38:41], v[30:31], off sc1
	global_load_dwordx4 v[10:13], v[48:49], off sc1
	global_load_dwordx4 v[26:29], v[46:47], off sc1
	v_lshlrev_b32_e32 v71, 2, v0
	v_bfe_u32 v30, v0, 3, 2
	v_and_b32_e32 v32, 28, v71
	v_lshlrev_b32_e32 v98, 9, v1
	v_or_b32_e32 v99, v32, v30
	v_bitop3_b32 v30, v70, v32, v30 bitop3:0x1e
	v_or_b32_e32 v33, 20, v70
	v_lshl_or_b32 v100, v30, 2, v98
	v_or_b32_e32 v30, 1, v50
	v_lshlrev_b32_e32 v69, 1, v33
	v_mul_hi_u32_u24_e32 v33, s6, v30
	v_mul_u32_u24_e32 v32, s6, v30
	v_mov_b32_e32 v31, v55
	v_lshl_add_u64 v[50:51], v[32:33], 2, v[56:57]
	v_mov_b32_e32 v33, v55
	v_mul_u32_u24_e32 v47, s6, v69
	global_load_dwordx4 v[72:75], v[50:51], off sc1
	v_lshlrev_b32_e32 v30, 2, v47
	v_bitop3_b32 v46, v70, v99, 4 bitop3:0x36
	v_lshl_add_u64 v[30:31], v[56:57], 0, v[30:31]
	v_lshl_or_b32 v101, v46, 2, v98
	global_load_dwordx4 v[46:49], v[30:31], off sc1
	v_or_b32_e32 v32, 28, v70
	v_lshlrev_b32_e32 v82, 1, v32
	v_mul_u32_u24_e32 v32, s6, v82
	v_lshlrev_b32_e32 v32, 2, v32
	s_waitcnt vmcnt(11)
	v_mov_b32_e32 v52, v18
	s_waitcnt vmcnt(10)
	v_mov_b32_e32 v53, v6
	v_mov_b32_e32 v58, v19
	v_mov_b32_e32 v59, v7
	v_pk_add_f32 v[62:63], v[52:53], v[58:59]
	v_pk_mul_f32 v[58:59], v[58:59], v[58:59]
	v_mov_b32_e32 v60, v20
	v_mov_b32_e32 v61, v8
	v_mov_b32_e32 v66, v21
	v_mov_b32_e32 v67, v9
	v_pk_fma_f32 v[52:53], v[52:53], v[52:53], v[58:59]
	s_waitcnt vmcnt(9)
	v_cvt_pk_bf16_f32 v19, v19, v15
	v_pk_add_f32 v[64:65], v[60:61], v[66:67]
	v_pk_fma_f32 v[52:53], v[60:61], v[60:61], v[52:53]
	v_mov_b32_e32 v60, v14
	v_cvt_pk_bf16_f32 v14, v18, v14
	ds_write2_b32 v100, v14, v19 offset1:32
	v_bitop3_b32 v14, v70, v99, 8 bitop3:0x36
	s_waitcnt vmcnt(8)
	v_mov_b32_e32 v61, v2
	v_cvt_pk_bf16_f32 v2, v6, v2
	v_lshl_or_b32 v55, v14, 2, v98
	v_cvt_pk_bf16_f32 v6, v7, v3
	ds_write2_b32 v55, v2, v6 offset1:32
	v_or_b32_e32 v2, 1, v68
	v_mul_hi_u32_u24_e32 v7, s6, v2
	v_mul_u32_u24_e32 v6, s6, v2
	v_lshl_add_u64 v[6:7], v[6:7], 2, v[56:57]
	v_pk_fma_f32 v[58:59], v[66:67], v[66:67], v[52:53]
	global_load_dwordx4 v[50:53], v[6:7], off sc1
	s_waitcnt vmcnt(8)
	v_mov_b32_e32 v86, v43
	s_waitcnt vmcnt(7)
	v_mov_b32_e32 v87, v23
	v_mov_b32_e32 v84, v42
	v_mov_b32_e32 v85, v22
	v_pk_mul_f32 v[6:7], v[86:87], v[86:87]
	v_bitop3_b32 v2, v70, v99, 12 bitop3:0x36
	v_mov_b32_e32 v88, v44
	v_mov_b32_e32 v89, v24
	v_pk_fma_f32 v[6:7], v[84:85], v[84:85], v[6:7]
	v_lshl_or_b32 v102, v2, 2, v98
	v_bitop3_b32 v2, v70, v99, 16 bitop3:0x36
	v_mov_b32_e32 v90, v45
	v_mov_b32_e32 v91, v25
	v_pk_fma_f32 v[6:7], v[88:89], v[88:89], v[6:7]
	v_lshl_or_b32 v103, v2, 2, v98
	v_or_b32_e32 v2, 1, v69
	v_lshl_add_u64 v[30:31], v[56:57], 0, v[32:33]
	v_pk_fma_f32 v[92:93], v[90:91], v[90:91], v[6:7]
	v_mul_hi_u32_u24_e32 v7, s6, v2
	v_mul_u32_u24_e32 v6, s6, v2
	v_bitop3_b32 v2, v70, v99, 20 bitop3:0x36
	global_load_dwordx4 v[30:33], v[30:31], off sc1
	v_lshl_add_u64 v[76:77], v[6:7], 2, v[56:57]
	v_lshl_or_b32 v104, v2, 2, v98
	s_waitcnt vmcnt(6)
	v_mov_b32_e32 v6, v38
	s_waitcnt vmcnt(4)
	v_mov_b32_e32 v7, v26
	v_mov_b32_e32 v18, v39
	v_mov_b32_e32 v19, v27
	v_bitop3_b32 v2, v70, v99, 24 bitop3:0x36
	v_pk_add_f32 v[66:67], v[6:7], v[18:19]
	v_pk_mul_f32 v[18:19], v[18:19], v[18:19]
	v_lshl_or_b32 v107, v2, 2, v98
	v_or_b32_e32 v2, 1, v82
	v_mov_b32_e32 v78, v40
	v_mov_b32_e32 v79, v28
	v_pk_fma_f32 v[6:7], v[6:7], v[6:7], v[18:19]
	v_cvt_pk_bf16_f32 v106, v26, v10
	v_cvt_pk_bf16_f32 v108, v27, v11
	v_mul_hi_u32_u24_e32 v27, s6, v2
	v_mul_u32_u24_e32 v26, s6, v2
	v_mov_b32_e32 v80, v41
	v_mov_b32_e32 v81, v29
	v_pk_fma_f32 v[6:7], v[78:79], v[78:79], v[6:7]
	v_lshl_add_u64 v[26:27], v[26:27], 2, v[56:57]
	v_pk_add_f32 v[68:69], v[78:79], v[80:81]
	v_pk_fma_f32 v[6:7], v[80:81], v[80:81], v[6:7]
	global_load_dwordx4 v[76:79], v[76:77], off sc1
	v_bitop3_b32 v2, v70, v99, 28 bitop3:0x36
	global_load_dwordx4 v[80:83], v[26:27], off sc1
	v_lshl_or_b32 v98, v2, 2, v98
	v_mbcnt_lo_u32_b32 v2, -1, 0
	v_mbcnt_hi_u32_b32 v2, -1, v2
	v_mov_b32_e32 v19, v10
	v_and_b32_e32 v10, 64, v2
	v_add_u32_e32 v10, 64, v10
	v_xor_b32_e32 v14, 32, v2
	v_cmp_lt_i32_e32 vcc, v14, v10
	v_cvt_pk_bf16_f32 v111, v21, v17
	v_mov_b32_e32 v21, v4
	v_cndmask_b32_e32 v14, v2, v14, vcc
	v_lshlrev_b32_e32 v99, 2, v14
	v_xor_b32_e32 v14, 16, v2
	v_cmp_lt_i32_e32 vcc, v14, v10
	v_cvt_pk_bf16_f32 v4, v8, v4
	v_pk_add_f32 v[62:63], v[62:63], v[64:65]
	v_cndmask_b32_e32 v14, v2, v14, vcc
	v_lshlrev_b32_e32 v109, 2, v14
	v_xor_b32_e32 v14, 8, v2
	v_cmp_lt_i32_e32 vcc, v14, v10
	s_waitcnt vmcnt(4)
	v_mov_b32_e32 v26, v47
	v_cvt_pk_bf16_f32 v105, v39, v35
	v_cndmask_b32_e32 v14, v2, v14, vcc
	v_lshlrev_b32_e32 v110, 2, v14
	v_cvt_pk_bf16_f32 v14, v20, v16
	v_xor_b32_e32 v20, 4, v2
	v_cmp_lt_i32_e32 vcc, v20, v10
	ds_write2_b32 v100, v14, v111 offset0:64 offset1:96
	v_mov_b32_e32 v18, v34
	v_cndmask_b32_e32 v20, v2, v20, vcc
	v_lshlrev_b32_e32 v112, 2, v20
	v_xor_b32_e32 v20, 2, v2
	v_cmp_lt_i32_e32 vcc, v20, v10
	v_cvt_pk_bf16_f32 v34, v38, v34
	v_mov_b32_e32 v38, v46
	v_cndmask_b32_e32 v20, v2, v20, vcc
	v_lshlrev_b32_e32 v113, 2, v20
	v_xor_b32_e32 v20, 1, v2
	v_cmp_lt_i32_e32 vcc, v20, v10
	v_cvt_pk_bf16_f32 v10, v43, v73
	s_waitcnt vmcnt(3)
	v_mov_b32_e32 v43, v50
	v_cndmask_b32_e32 v2, v2, v20, vcc
	v_lshlrev_b32_e32 v114, 2, v2
	v_cvt_pk_bf16_f32 v2, v42, v72
	ds_write2_b32 v101, v2, v10 offset1:32
	v_cvt_pk_bf16_f32 v2, v44, v74
	v_cvt_pk_bf16_f32 v10, v45, v75
	v_mov_b32_e32 v20, v16
	v_mov_b32_e32 v16, v17
	v_mov_b32_e32 v17, v5
	ds_write2_b32 v101, v2, v10 offset0:64 offset1:96
	v_mov_b32_e32 v2, v15
	v_cvt_pk_bf16_f32 v5, v9, v5
	v_mov_b32_e32 v42, v72
	v_mov_b32_e32 v44, v73
	v_mov_b32_e32 v45, v51
	v_pk_add_f32 v[14:15], v[60:61], v[2:3]
	ds_write2_b32 v55, v4, v5 offset0:64 offset1:96
	v_pk_add_f32 v[4:5], v[84:85], v[86:87]
	v_pk_add_f32 v[8:9], v[88:89], v[90:91]
	v_mov_b32_e32 v72, v74
	v_mov_b32_e32 v73, v52
	v_mov_b32_e32 v74, v75
	v_mov_b32_e32 v75, v53
	v_pk_add_f32 v[14:15], v[62:63], v[14:15]
	v_pk_add_f32 v[62:63], v[20:21], v[16:17]
	v_pk_add_f32 v[4:5], v[4:5], v[8:9]
	v_pk_add_f32 v[8:9], v[42:43], v[44:45]
	v_pk_add_f32 v[14:15], v[14:15], v[62:63]
	v_pk_add_f32 v[4:5], v[4:5], v[8:9]
	v_pk_add_f32 v[8:9], v[72:73], v[74:75]
	v_pk_add_f32 v[14:15], v[14:15], 0 op_sel_hi:[1,0]
	v_pk_add_f32 v[4:5], v[4:5], v[8:9]
	v_cvt_pk_bf16_f32 v10, v22, v50
	v_pk_add_f32 v[4:5], v[14:15], v[4:5]
	v_pk_fma_f32 v[14:15], v[60:61], v[60:61], v[58:59]
	ds_bpermute_b32 v8, v99, v4
	v_pk_fma_f32 v[2:3], v[2:3], v[2:3], v[14:15]
	v_pk_fma_f32 v[14:15], v[42:43], v[42:43], v[92:93]
	v_pk_fma_f32 v[2:3], v[20:21], v[20:21], v[2:3]
	v_pk_fma_f32 v[14:15], v[44:45], v[44:45], v[14:15]
	v_pk_fma_f32 v[2:3], v[16:17], v[16:17], v[2:3]
	v_pk_fma_f32 v[14:15], v[72:73], v[72:73], v[14:15]
	ds_bpermute_b32 v9, v99, v5
	v_pk_fma_f32 v[14:15], v[74:75], v[74:75], v[14:15]
	v_cvt_pk_bf16_f32 v16, v23, v51
	v_pk_add_f32 v[2:3], v[2:3], v[14:15]
	ds_bpermute_b32 v14, v99, v2
	ds_bpermute_b32 v15, v99, v3
	s_waitcnt lgkmcnt(0)
	v_pk_add_f32 v[4:5], v[4:5], v[8:9]
	ds_bpermute_b32 v8, v109, v4
	ds_bpermute_b32 v9, v109, v5
	s_waitcnt vmcnt(2)
	v_mov_b32_e32 v27, v31
	v_pk_add_f32 v[2:3], v[2:3], v[14:15]
	ds_bpermute_b32 v14, v109, v2
	ds_bpermute_b32 v15, v109, v3
	s_waitcnt lgkmcnt(2)
	v_pk_add_f32 v[4:5], v[4:5], v[8:9]
	ds_bpermute_b32 v8, v110, v4
	ds_bpermute_b32 v9, v110, v5
	ds_write2_b32 v102, v10, v16 offset1:32
	s_waitcnt lgkmcnt(3)
	v_pk_add_f32 v[2:3], v[2:3], v[14:15]
	ds_bpermute_b32 v14, v110, v2
	ds_bpermute_b32 v15, v110, v3
	s_waitcnt lgkmcnt(3)
	v_pk_add_f32 v[4:5], v[4:5], v[8:9]
	ds_bpermute_b32 v8, v112, v4
	ds_bpermute_b32 v9, v112, v5
	v_mov_b32_e32 v39, v30
	s_waitcnt lgkmcnt(2)
	v_pk_add_f32 v[2:3], v[2:3], v[14:15]
	ds_bpermute_b32 v14, v112, v2
	ds_bpermute_b32 v15, v112, v3
	s_waitcnt lgkmcnt(2)
	v_pk_add_f32 v[4:5], v[4:5], v[8:9]
	ds_bpermute_b32 v8, v113, v4
	ds_bpermute_b32 v9, v113, v5
	v_pk_mul_f32 v[96:97], v[26:27], v[26:27]
	s_waitcnt lgkmcnt(2)
	v_pk_add_f32 v[14:15], v[2:3], v[14:15]
	ds_bpermute_b32 v16, v113, v14
	ds_bpermute_b32 v17, v113, v15
	v_mov_b32_e32 v56, v48
	v_mov_b32_e32 v57, v32
	v_pk_fma_f32 v[96:97], v[38:39], v[38:39], v[96:97]
	v_mov_b32_e32 v94, v49
	v_mov_b32_e32 v95, v33
	v_pk_fma_f32 v[96:97], v[56:57], v[56:57], v[96:97]
	v_cvt_pk_bf16_f32 v10, v24, v52
	v_cvt_pk_bf16_f32 v20, v25, v53
	v_pk_fma_f32 v[96:97], v[94:95], v[94:95], v[96:97]
	ds_write2_b32 v102, v10, v20 offset0:64 offset1:96
	ds_write2_b32 v103, v34, v105 offset1:32
	s_waitcnt vmcnt(1)
	v_mov_b32_e32 v22, v76
	s_waitcnt vmcnt(0)
	v_mov_b32_e32 v23, v80
	v_mov_b32_e32 v10, v35
	v_pk_fma_f32 v[6:7], v[18:19], v[18:19], v[6:7]
	s_waitcnt lgkmcnt(4)
	v_pk_add_f32 v[2:3], v[4:5], v[8:9]
	s_waitcnt lgkmcnt(2)
	v_pk_add_f32 v[4:5], v[14:15], v[16:17]
	v_mov_b32_e32 v16, v36
	v_mov_b32_e32 v17, v12
	v_mov_b32_e32 v20, v37
	v_mov_b32_e32 v21, v13
	v_mov_b32_e32 v24, v77
	v_mov_b32_e32 v25, v81
	v_pk_add_f32 v[42:43], v[66:67], v[68:69]
	v_pk_add_f32 v[34:35], v[18:19], v[10:11]
	v_cvt_pk_bf16_f32 v28, v28, v12
	v_cvt_pk_bf16_f32 v29, v29, v13
	v_pk_add_f32 v[12:13], v[38:39], v[26:27]
	v_pk_add_f32 v[26:27], v[56:57], v[94:95]
	v_pk_fma_f32 v[6:7], v[10:11], v[10:11], v[6:7]
	v_pk_fma_f32 v[10:11], v[22:23], v[22:23], v[96:97]
	v_cvt_pk_bf16_f32 v44, v40, v36
	v_cvt_pk_bf16_f32 v45, v41, v37
	v_mov_b32_e32 v36, v78
	v_mov_b32_e32 v37, v82
	v_mov_b32_e32 v40, v79
	v_mov_b32_e32 v41, v83
	v_pk_add_f32 v[34:35], v[42:43], v[34:35]
	v_pk_add_f32 v[42:43], v[16:17], v[20:21]
	v_pk_add_f32 v[12:13], v[12:13], v[26:27]
	v_pk_add_f32 v[26:27], v[22:23], v[24:25]
	v_pk_fma_f32 v[10:11], v[24:25], v[24:25], v[10:11]
	v_pk_add_f32 v[34:35], v[34:35], v[42:43]
	v_pk_add_f32 v[12:13], v[12:13], v[26:27]
	v_pk_add_f32 v[26:27], v[36:37], v[40:41]
	v_pk_fma_f32 v[6:7], v[16:17], v[16:17], v[6:7]
	v_pk_fma_f32 v[10:11], v[36:37], v[36:37], v[10:11]
	v_pk_add_f32 v[34:35], v[34:35], 0 op_sel_hi:[1,0]
	v_pk_add_f32 v[12:13], v[12:13], v[26:27]
	v_pk_fma_f32 v[6:7], v[20:21], v[20:21], v[6:7]
	v_pk_fma_f32 v[10:11], v[40:41], v[40:41], v[10:11]
	v_pk_add_f32 v[12:13], v[34:35], v[12:13]
	v_pk_add_f32 v[6:7], v[6:7], v[10:11]
	ds_bpermute_b32 v26, v99, v12
	ds_bpermute_b32 v27, v99, v13
	ds_bpermute_b32 v10, v99, v6
	ds_bpermute_b32 v11, v99, v7
	ds_bpermute_b32 v8, v114, v2
	ds_bpermute_b32 v14, v114, v4
	s_waitcnt lgkmcnt(4)
	v_pk_add_f32 v[12:13], v[12:13], v[26:27]
	ds_bpermute_b32 v16, v109, v12
	s_waitcnt lgkmcnt(3)
	v_pk_add_f32 v[6:7], v[6:7], v[10:11]
	ds_bpermute_b32 v17, v109, v13
	ds_bpermute_b32 v10, v109, v6
	ds_bpermute_b32 v11, v109, v7
	ds_bpermute_b32 v9, v114, v3
	ds_bpermute_b32 v15, v114, v5
	s_waitcnt lgkmcnt(4)
	v_pk_add_f32 v[12:13], v[12:13], v[16:17]
	ds_bpermute_b32 v16, v110, v12
	s_waitcnt lgkmcnt(3)
	v_pk_add_f32 v[6:7], v[6:7], v[10:11]
	ds_bpermute_b32 v17, v110, v13
	ds_bpermute_b32 v10, v110, v6
	ds_bpermute_b32 v11, v110, v7
	v_cvt_pk_bf16_f32 v46, v46, v76
	v_cvt_pk_bf16_f32 v47, v47, v77
	s_waitcnt lgkmcnt(2)
	v_pk_add_f32 v[12:13], v[12:13], v[16:17]
	ds_bpermute_b32 v16, v112, v12
	s_waitcnt lgkmcnt(1)
	v_pk_add_f32 v[6:7], v[6:7], v[10:11]
	ds_bpermute_b32 v17, v112, v13
	ds_bpermute_b32 v10, v112, v6
	ds_bpermute_b32 v11, v112, v7
	v_cvt_pk_bf16_f32 v48, v48, v78
	v_cvt_pk_bf16_f32 v49, v49, v79
	s_waitcnt lgkmcnt(2)
	v_pk_add_f32 v[12:13], v[12:13], v[16:17]
	ds_bpermute_b32 v16, v113, v12
	s_waitcnt lgkmcnt(1)
	v_pk_add_f32 v[6:7], v[6:7], v[10:11]
	ds_bpermute_b32 v17, v113, v13
	ds_bpermute_b32 v10, v113, v6
	ds_bpermute_b32 v11, v113, v7
	v_cmp_eq_u32_e32 vcc, 0, v1
	v_cvt_pk_bf16_f32 v30, v30, v80
	s_waitcnt lgkmcnt(2)
	v_pk_add_f32 v[12:13], v[12:13], v[16:17]
	ds_bpermute_b32 v16, v114, v12
	s_waitcnt lgkmcnt(1)
	v_pk_add_f32 v[6:7], v[6:7], v[10:11]
	ds_bpermute_b32 v10, v114, v6
	ds_bpermute_b32 v17, v114, v13
	ds_bpermute_b32 v11, v114, v7
	v_cvt_pk_bf16_f32 v31, v31, v81
	v_cvt_pk_bf16_f32 v18, v32, v82
	v_cvt_pk_bf16_f32 v19, v33, v83
	ds_write2_b32 v103, v44, v45 offset0:64 offset1:96
	ds_write2_b32 v104, v46, v47 offset1:32
	ds_write2_b32 v104, v48, v49 offset0:64 offset1:96
	ds_write2_b32 v107, v106, v108 offset1:32
	ds_write2_b32 v107, v28, v29 offset0:64 offset1:96
	ds_write2_b32 v98, v30, v31 offset1:32
	ds_write2_b32 v98, v18, v19 offset0:64 offset1:96
	s_and_saveexec_b64 s[6:7], vcc
	s_cbranch_execz .LBB0_7
	v_lshlrev_b32_e32 v18, 5, v70
	v_pk_add_f32 v[2:3], v[2:3], v[8:9]
	v_pk_add_f32 v[8:9], v[4:5], v[14:15]
	s_waitcnt lgkmcnt(8)
	v_pk_add_f32 v[4:5], v[12:13], v[16:17]
	s_waitcnt lgkmcnt(7)
	v_pk_add_f32 v[10:11], v[6:7], v[10:11]
	ds_write_b128 v18, v[2:5] offset:32768
	ds_write_b128 v18, v[8:11] offset:32784
